# attention unit epilogue (4 mixers): the 16 per-row 1/l LDS reads issued together with one wait instead of 16 serialized read+wait round trips
# speedup vs baseline: 1.0110x; 1.0073x over previous
.LBB0_515:
	s_or_b64 exec, exec, s[0:1]
	s_waitcnt lgkmcnt(0)
	ds_read_b32 v83, v168 offset:49152
	ds_read_b32 v84, v168 offset:49156
	ds_read_b32 v85, v168 offset:49160
	ds_read_b32 v86, v168 offset:49164
	ds_read_b32 v87, v168 offset:49184
	ds_read_b32 v88, v168 offset:49188
	ds_read_b32 v89, v168 offset:49192
	ds_read_b32 v90, v168 offset:49196
	ds_read_b32 v92, v168 offset:49216
	ds_read_b32 v94, v168 offset:49220
	ds_read_b32 v96, v168 offset:49224
	ds_read_b32 v97, v168 offset:49228
	ds_read_b32 v98, v168 offset:49248
	ds_read_b32 v100, v168 offset:49252
	ds_read_b32 v102, v168 offset:49256
	ds_read_b32 v103, v168 offset:49260
	v_add_u32_e32 v33, v169, v170
	s_lshl_b32 s0, s29, 10
	v_readlane_b32 s1, v254, 48
	s_add_u32 s0, s1, s0
	s_waitcnt lgkmcnt(0)
	v_mul_f32_e32 v0, v0, v83
	v_cvt_pk_bf16_f32 v0, v0, v117
	ds_write_b16 v33, v0 offset:51200
	v_mul_f32_e32 v0, v16, v83
	v_cvt_pk_bf16_f32 v0, v0, v117
	ds_write_b16 v33, v0 offset:51264
	v_readlane_b32 s1, v254, 49
	s_addc_u32 s1, s1, 0
	s_add_u32 s0, s0, s31
	s_addc_u32 s1, s1, 0
	v_mul_f32_e32 v1, v1, v84
	v_mul_f32_e32 v0, v17, v84
	v_cvt_pk_bf16_f32 v1, v1, v117
	ds_write_b16 v172, v1 offset:51200
	v_cvt_pk_bf16_f32 v0, v0, v117
	ds_write_b16 v172, v0 offset:51264
	s_lshl_b64 s[6:7], s[8:9], 10
	s_add_u32 s0, s0, s6
	s_addc_u32 s1, s1, s7
	v_mul_f32_e32 v1, v2, v85
	v_mul_f32_e32 v0, v18, v85
	v_cvt_pk_bf16_f32 v1, v1, v117
	ds_write_b16 v173, v1 offset:51200
	v_cvt_pk_bf16_f32 v0, v0, v117
	ds_write_b16 v173, v0 offset:51264
	v_mul_f32_e32 v1, v3, v86
	v_mul_f32_e32 v0, v19, v86
	v_cvt_pk_bf16_f32 v1, v1, v117
	ds_write_b16 v174, v1 offset:51200
	v_cvt_pk_bf16_f32 v0, v0, v117
	ds_write_b16 v174, v0 offset:51264
	v_mul_f32_e32 v1, v4, v87
	v_mul_f32_e32 v0, v20, v87
	v_cvt_pk_bf16_f32 v1, v1, v117
	ds_write_b16 v175, v1 offset:51200
	v_cvt_pk_bf16_f32 v0, v0, v117
	ds_write_b16 v175, v0 offset:51264
	v_mul_f32_e32 v1, v5, v88
	v_mul_f32_e32 v0, v21, v88
	v_cvt_pk_bf16_f32 v1, v1, v117
	ds_write_b16 v176, v1 offset:51200
	v_cvt_pk_bf16_f32 v0, v0, v117
	ds_write_b16 v176, v0 offset:51264
	v_mul_f32_e32 v1, v6, v89
	v_mul_f32_e32 v0, v22, v89
	v_cvt_pk_bf16_f32 v1, v1, v117
	ds_write_b16 v177, v1 offset:51200
	v_cvt_pk_bf16_f32 v0, v0, v117
	ds_write_b16 v177, v0 offset:51264
	v_mul_f32_e32 v1, v7, v90
	v_mul_f32_e32 v0, v23, v90
	v_cvt_pk_bf16_f32 v1, v1, v117
	ds_write_b16 v178, v1 offset:51200
	v_cvt_pk_bf16_f32 v0, v0, v117
	ds_write_b16 v178, v0 offset:51264
	v_mul_f32_e32 v1, v8, v92
	v_mul_f32_e32 v0, v24, v92
	v_cvt_pk_bf16_f32 v1, v1, v117
	ds_write_b16 v179, v1 offset:51200
	v_cvt_pk_bf16_f32 v0, v0, v117
	ds_write_b16 v179, v0 offset:51264
	v_mul_f32_e32 v1, v9, v94
	v_mul_f32_e32 v0, v25, v94
	v_cvt_pk_bf16_f32 v1, v1, v117
	ds_write_b16 v180, v1 offset:51200
	v_cvt_pk_bf16_f32 v0, v0, v117
	ds_write_b16 v180, v0 offset:51264
	v_mul_f32_e32 v1, v10, v96
	v_mul_f32_e32 v0, v26, v96
	v_cvt_pk_bf16_f32 v1, v1, v117
	ds_write_b16 v181, v1 offset:51200
	v_cvt_pk_bf16_f32 v0, v0, v117
	ds_write_b16 v181, v0 offset:51264
	v_mul_f32_e32 v1, v11, v97
	v_mul_f32_e32 v0, v27, v97
	v_cvt_pk_bf16_f32 v1, v1, v117
	ds_write_b16 v182, v1 offset:51200
	v_cvt_pk_bf16_f32 v0, v0, v117
	ds_write_b16 v182, v0 offset:51264
	v_mul_f32_e32 v1, v12, v98
	v_mul_f32_e32 v0, v28, v98
	v_cvt_pk_bf16_f32 v1, v1, v117
	ds_write_b16 v183, v1 offset:51200
	v_cvt_pk_bf16_f32 v0, v0, v117
	ds_write_b16 v183, v0 offset:51264
	v_mul_f32_e32 v1, v13, v100
	v_mul_f32_e32 v0, v29, v100
	v_cvt_pk_bf16_f32 v1, v1, v117
	ds_write_b16 v184, v1 offset:51200
	v_cvt_pk_bf16_f32 v0, v0, v117
	ds_write_b16 v184, v0 offset:51264
	v_mul_f32_e32 v1, v14, v102
	v_mul_f32_e32 v0, v30, v102
	v_cvt_pk_bf16_f32 v1, v1, v117
	ds_write_b16 v185, v1 offset:51200
	v_cvt_pk_bf16_f32 v0, v0, v117
	ds_write_b16 v185, v0 offset:51264
	v_mul_f32_e32 v1, v15, v103
	v_mul_f32_e32 v0, v31, v103
	v_cvt_pk_bf16_f32 v1, v1, v117
	ds_write_b16 v186, v1 offset:51200
	v_cvt_pk_bf16_f32 v0, v0, v117
	ds_write_b16 v186, v0 offset:51264
	s_waitcnt lgkmcnt(0)
	ds_read_b128 v[2:5], v187 offset:51200
	v_lshl_add_u64 v[0:1], s[0:1], 0, v[122:123]
	s_waitcnt lgkmcnt(0)
	v_lshlrev_b32_e32 v6, 16, v2
	v_and_b32_e32 v2, 0xffff0000, v2
	v_lshlrev_b32_e32 v8, 16, v4
	v_and_b32_e32 v4, 0xffff0000, v4
	v_mul_f32_e32 v2, 0x41800000, v2
	v_lshlrev_b32_e32 v7, 16, v3
	v_med3_f32 v10, v2, s28, v193
	v_mul_f32_e32 v2, 0x41800000, v4
	v_lshlrev_b32_e32 v9, 16, v5
	v_med3_f32 v4, v2, s28, v193
	v_mul_f32_e32 v2, 0x41800000, v7
	v_and_b32_e32 v3, 0xffff0000, v3
	v_med3_f32 v7, v2, s28, v193
	v_mul_f32_e32 v2, 0x41800000, v9
	v_and_b32_e32 v5, 0xffff0000, v5
	v_med3_f32 v9, v2, s28, v193
	v_mul_f32_e32 v2, 0x41800000, v3
	v_mul_f32_e32 v6, 0x41800000, v6
	v_med3_f32 v3, v2, s28, v193
	v_mul_f32_e32 v2, 0x41800000, v5
	v_med3_f32 v6, v6, s28, v193
	v_med3_f32 v5, v2, s28, v193
	v_mov_b32_e32 v2, 0
	v_cvt_pk_fp8_f32 v2, v6, v10
	v_mul_f32_e32 v8, 0x41800000, v8
	v_med3_f32 v8, v8, s28, v193
	v_cvt_pk_fp8_f32 v2, v7, v3 op_sel:[0,0,1]
	v_mov_b32_e32 v3, 0
	v_cvt_pk_fp8_f32 v3, v8, v4
	v_cvt_pk_fp8_f32 v3, v9, v5 op_sel:[0,0,1]
	v_lshl_add_u64 v[4:5], v[0:1], 0, v[124:125]
	global_store_dwordx2 v[4:5], v[2:3], off
	ds_read_b128 v[2:5], v188 offset:51200
	s_waitcnt lgkmcnt(0)
	v_lshlrev_b32_e32 v6, 16, v2
	v_and_b32_e32 v2, 0xffff0000, v2
	v_lshlrev_b32_e32 v8, 16, v4
	v_and_b32_e32 v4, 0xffff0000, v4
	v_mul_f32_e32 v2, 0x41800000, v2
	v_lshlrev_b32_e32 v7, 16, v3
	v_med3_f32 v10, v2, s28, v193
	v_mul_f32_e32 v2, 0x41800000, v4
	v_lshlrev_b32_e32 v9, 16, v5
	v_med3_f32 v4, v2, s28, v193
	v_mul_f32_e32 v2, 0x41800000, v7
	v_and_b32_e32 v3, 0xffff0000, v3
	v_med3_f32 v7, v2, s28, v193
	v_mul_f32_e32 v2, 0x41800000, v9
	v_and_b32_e32 v5, 0xffff0000, v5
	v_med3_f32 v9, v2, s28, v193
	v_mul_f32_e32 v2, 0x41800000, v3
	v_mul_f32_e32 v6, 0x41800000, v6
	v_med3_f32 v3, v2, s28, v193
	v_mul_f32_e32 v2, 0x41800000, v5
	v_med3_f32 v6, v6, s28, v193
	v_med3_f32 v5, v2, s28, v193
	v_mov_b32_e32 v2, 0
	v_cvt_pk_fp8_f32 v2, v6, v10
	v_mul_f32_e32 v8, 0x41800000, v8
	v_med3_f32 v8, v8, s28, v193
	v_cvt_pk_fp8_f32 v2, v7, v3 op_sel:[0,0,1]
	v_mov_b32_e32 v3, 0
	v_cvt_pk_fp8_f32 v3, v8, v4
	v_cvt_pk_fp8_f32 v3, v9, v5 op_sel:[0,0,1]
	v_lshl_add_u64 v[4:5], v[0:1], 0, v[126:127]
	global_store_dwordx2 v[4:5], v[2:3], off
	ds_read_b128 v[2:5], v189 offset:51200
	s_waitcnt lgkmcnt(0)
	v_lshlrev_b32_e32 v6, 16, v2
	v_and_b32_e32 v2, 0xffff0000, v2
	v_lshlrev_b32_e32 v8, 16, v4
	v_and_b32_e32 v4, 0xffff0000, v4
	v_mul_f32_e32 v2, 0x41800000, v2
	v_lshlrev_b32_e32 v7, 16, v3
	v_med3_f32 v10, v2, s28, v193
	v_mul_f32_e32 v2, 0x41800000, v4
	v_lshlrev_b32_e32 v9, 16, v5
	v_med3_f32 v4, v2, s28, v193
	v_mul_f32_e32 v2, 0x41800000, v7
	v_and_b32_e32 v3, 0xffff0000, v3
	v_med3_f32 v7, v2, s28, v193
	v_mul_f32_e32 v2, 0x41800000, v9
	v_and_b32_e32 v5, 0xffff0000, v5
	v_med3_f32 v9, v2, s28, v193
	v_mul_f32_e32 v2, 0x41800000, v3
	v_mul_f32_e32 v6, 0x41800000, v6
	v_med3_f32 v3, v2, s28, v193
	v_mul_f32_e32 v2, 0x41800000, v5
	v_med3_f32 v6, v6, s28, v193
	v_med3_f32 v5, v2, s28, v193
	v_mov_b32_e32 v2, 0
	v_cvt_pk_fp8_f32 v2, v6, v10
	v_mul_f32_e32 v8, 0x41800000, v8
	v_med3_f32 v8, v8, s28, v193
	v_cvt_pk_fp8_f32 v2, v7, v3 op_sel:[0,0,1]
	v_mov_b32_e32 v3, 0
	v_cvt_pk_fp8_f32 v3, v8, v4
	v_cvt_pk_fp8_f32 v3, v9, v5 op_sel:[0,0,1]
	v_lshl_add_u64 v[4:5], v[0:1], 0, v[128:129]
	v_lshl_add_u64 v[0:1], v[0:1], 0, v[130:131]
	global_store_dwordx2 v[4:5], v[2:3], off
	ds_read_b128 v[2:5], v190 offset:51200
	s_waitcnt lgkmcnt(0)
	v_lshlrev_b32_e32 v6, 16, v2
	v_and_b32_e32 v2, 0xffff0000, v2
	v_lshlrev_b32_e32 v8, 16, v4
	v_and_b32_e32 v4, 0xffff0000, v4
	v_mul_f32_e32 v2, 0x41800000, v2
	v_lshlrev_b32_e32 v7, 16, v3
	v_med3_f32 v10, v2, s28, v193
	v_mul_f32_e32 v2, 0x41800000, v4
	v_lshlrev_b32_e32 v9, 16, v5
	v_med3_f32 v4, v2, s28, v193
	v_mul_f32_e32 v2, 0x41800000, v7
	v_and_b32_e32 v3, 0xffff0000, v3
	v_med3_f32 v7, v2, s28, v193
	v_mul_f32_e32 v2, 0x41800000, v9
	v_and_b32_e32 v5, 0xffff0000, v5
	v_med3_f32 v9, v2, s28, v193
	v_mul_f32_e32 v2, 0x41800000, v3
	v_mul_f32_e32 v6, 0x41800000, v6
	v_med3_f32 v3, v2, s28, v193
	v_mul_f32_e32 v2, 0x41800000, v5
	v_med3_f32 v6, v6, s28, v193
	v_med3_f32 v5, v2, s28, v193
	v_mov_b32_e32 v2, 0
	v_cvt_pk_fp8_f32 v2, v6, v10
	v_mul_f32_e32 v8, 0x41800000, v8
	v_med3_f32 v8, v8, s28, v193
	v_cvt_pk_fp8_f32 v2, v7, v3 op_sel:[0,0,1]
	v_mov_b32_e32 v3, 0
	v_cvt_pk_fp8_f32 v3, v8, v4
	v_cvt_pk_fp8_f32 v3, v9, v5 op_sel:[0,0,1]
	global_store_dwordx2 v[0:1], v[2:3], off
	s_waitcnt lgkmcnt(0)
	s_barrier
	s_and_saveexec_b64 s[0:1], s[2:3]
	s_cbranch_execz .LBB0_465
	v_mov_b32_e32 v0, s16
	ds_write_b32 v0, v194
	s_branch .LBB0_465

.LBB0_1427:
	s_or_b64 exec, exec, s[38:39]
	s_waitcnt lgkmcnt(0)
	ds_read_b32 v83, v160 offset:49152
	ds_read_b32 v84, v160 offset:49156
	ds_read_b32 v85, v160 offset:49160
	ds_read_b32 v86, v160 offset:49164
	ds_read_b32 v87, v160 offset:49184
	ds_read_b32 v88, v160 offset:49188
	ds_read_b32 v89, v160 offset:49192
	ds_read_b32 v90, v160 offset:49196
	ds_read_b32 v92, v160 offset:49216
	ds_read_b32 v94, v160 offset:49220
	ds_read_b32 v96, v160 offset:49224
	ds_read_b32 v97, v160 offset:49228
	ds_read_b32 v98, v160 offset:49248
	ds_read_b32 v100, v160 offset:49252
	ds_read_b32 v102, v160 offset:49256
	ds_read_b32 v103, v160 offset:49260
	v_add_u32_e32 v33, v161, v162
	s_lshl_b32 s38, s40, 10
	v_readlane_b32 s39, v254, 48
	s_add_u32 s38, s39, s38
	s_waitcnt lgkmcnt(0)
	v_mul_f32_e32 v0, v0, v83
	v_cvt_pk_bf16_f32 v0, v0, v117
	ds_write_b16 v33, v0 offset:51200
	v_mul_f32_e32 v0, v16, v83
	v_cvt_pk_bf16_f32 v0, v0, v117
	ds_write_b16 v33, v0 offset:51264
	v_readlane_b32 s39, v254, 49
	s_addc_u32 s39, s39, 0
	s_add_u32 s38, s38, s41
	s_addc_u32 s39, s39, 0
	v_mul_f32_e32 v1, v1, v84
	v_mul_f32_e32 v0, v17, v84
	v_cvt_pk_bf16_f32 v1, v1, v117
	ds_write_b16 v165, v1 offset:51200
	v_cvt_pk_bf16_f32 v0, v0, v117
	ds_write_b16 v165, v0 offset:51264
	s_lshl_b64 s[40:41], s[0:1], 10
	s_add_u32 s38, s38, s40
	s_addc_u32 s39, s39, s41
	v_mul_f32_e32 v1, v2, v85
	v_mul_f32_e32 v0, v18, v85
	v_cvt_pk_bf16_f32 v1, v1, v117
	ds_write_b16 v166, v1 offset:51200
	v_cvt_pk_bf16_f32 v0, v0, v117
	ds_write_b16 v166, v0 offset:51264
	v_mul_f32_e32 v1, v3, v86
	v_mul_f32_e32 v0, v19, v86
	v_cvt_pk_bf16_f32 v1, v1, v117
	ds_write_b16 v167, v1 offset:51200
	v_cvt_pk_bf16_f32 v0, v0, v117
	ds_write_b16 v167, v0 offset:51264
	v_mul_f32_e32 v1, v4, v87
	v_mul_f32_e32 v0, v20, v87
	v_cvt_pk_bf16_f32 v1, v1, v117
	ds_write_b16 v168, v1 offset:51200
	v_cvt_pk_bf16_f32 v0, v0, v117
	ds_write_b16 v168, v0 offset:51264
	v_mul_f32_e32 v1, v5, v88
	v_mul_f32_e32 v0, v21, v88
	v_cvt_pk_bf16_f32 v1, v1, v117
	ds_write_b16 v169, v1 offset:51200
	v_cvt_pk_bf16_f32 v0, v0, v117
	ds_write_b16 v169, v0 offset:51264
	v_mul_f32_e32 v1, v6, v89
	v_mul_f32_e32 v0, v22, v89
	v_cvt_pk_bf16_f32 v1, v1, v117
	ds_write_b16 v170, v1 offset:51200
	v_cvt_pk_bf16_f32 v0, v0, v117
	ds_write_b16 v170, v0 offset:51264
	v_mul_f32_e32 v1, v7, v90
	v_mul_f32_e32 v0, v23, v90
	v_cvt_pk_bf16_f32 v1, v1, v117
	ds_write_b16 v171, v1 offset:51200
	v_cvt_pk_bf16_f32 v0, v0, v117
	ds_write_b16 v171, v0 offset:51264
	v_mul_f32_e32 v1, v8, v92
	v_mul_f32_e32 v0, v24, v92
	v_cvt_pk_bf16_f32 v1, v1, v117
	ds_write_b16 v172, v1 offset:51200
	v_cvt_pk_bf16_f32 v0, v0, v117
	ds_write_b16 v172, v0 offset:51264
	v_mul_f32_e32 v1, v9, v94
	v_mul_f32_e32 v0, v25, v94
	v_cvt_pk_bf16_f32 v1, v1, v117
	ds_write_b16 v173, v1 offset:51200
	v_cvt_pk_bf16_f32 v0, v0, v117
	ds_write_b16 v173, v0 offset:51264
	v_mul_f32_e32 v1, v10, v96
	v_mul_f32_e32 v0, v26, v96
	v_cvt_pk_bf16_f32 v1, v1, v117
	ds_write_b16 v174, v1 offset:51200
	v_cvt_pk_bf16_f32 v0, v0, v117
	ds_write_b16 v174, v0 offset:51264
	v_mul_f32_e32 v1, v11, v97
	v_mul_f32_e32 v0, v27, v97
	v_cvt_pk_bf16_f32 v1, v1, v117
	ds_write_b16 v175, v1 offset:51200
	v_cvt_pk_bf16_f32 v0, v0, v117
	ds_write_b16 v175, v0 offset:51264
	v_mul_f32_e32 v1, v12, v98
	v_mul_f32_e32 v0, v28, v98
	v_cvt_pk_bf16_f32 v1, v1, v117
	ds_write_b16 v176, v1 offset:51200
	v_cvt_pk_bf16_f32 v0, v0, v117
	ds_write_b16 v176, v0 offset:51264
	v_mul_f32_e32 v1, v13, v100
	v_mul_f32_e32 v0, v29, v100
	v_cvt_pk_bf16_f32 v1, v1, v117
	ds_write_b16 v177, v1 offset:51200
	v_cvt_pk_bf16_f32 v0, v0, v117
	ds_write_b16 v177, v0 offset:51264
	v_mul_f32_e32 v1, v14, v102
	v_mul_f32_e32 v0, v30, v102
	v_cvt_pk_bf16_f32 v1, v1, v117
	ds_write_b16 v178, v1 offset:51200
	v_cvt_pk_bf16_f32 v0, v0, v117
	ds_write_b16 v178, v0 offset:51264
	v_mul_f32_e32 v1, v15, v103
	v_mul_f32_e32 v0, v31, v103
	v_cvt_pk_bf16_f32 v1, v1, v117
	ds_write_b16 v179, v1 offset:51200
	v_cvt_pk_bf16_f32 v0, v0, v117
	ds_write_b16 v179, v0 offset:51264
	s_waitcnt lgkmcnt(0)
	ds_read_b128 v[2:5], v180 offset:51200
	v_lshl_add_u64 v[0:1], s[38:39], 0, v[120:121]
	s_waitcnt lgkmcnt(0)
	v_lshlrev_b32_e32 v6, 16, v2
	v_and_b32_e32 v2, 0xffff0000, v2
	v_lshlrev_b32_e32 v8, 16, v4
	v_and_b32_e32 v4, 0xffff0000, v4
	v_mul_f32_e32 v2, 0x41800000, v2
	v_lshlrev_b32_e32 v7, 16, v3
	v_med3_f32 v10, v2, s33, v187
	v_mul_f32_e32 v2, 0x41800000, v4
	v_lshlrev_b32_e32 v9, 16, v5
	v_med3_f32 v4, v2, s33, v187
	v_mul_f32_e32 v2, 0x41800000, v7
	v_and_b32_e32 v3, 0xffff0000, v3
	v_med3_f32 v7, v2, s33, v187
	v_mul_f32_e32 v2, 0x41800000, v9
	v_and_b32_e32 v5, 0xffff0000, v5
	v_med3_f32 v9, v2, s33, v187
	v_mul_f32_e32 v2, 0x41800000, v3
	v_mul_f32_e32 v6, 0x41800000, v6
	v_med3_f32 v3, v2, s33, v187
	v_mul_f32_e32 v2, 0x41800000, v5
	v_med3_f32 v6, v6, s33, v187
	v_med3_f32 v5, v2, s33, v187
	v_mov_b32_e32 v2, 0
	v_cvt_pk_fp8_f32 v2, v6, v10
	v_mul_f32_e32 v8, 0x41800000, v8
	v_med3_f32 v8, v8, s33, v187
	v_cvt_pk_fp8_f32 v2, v7, v3 op_sel:[0,0,1]
	v_mov_b32_e32 v3, 0
	v_cvt_pk_fp8_f32 v3, v8, v4
	v_cvt_pk_fp8_f32 v3, v9, v5 op_sel:[0,0,1]
	v_lshl_add_u64 v[4:5], v[0:1], 0, v[122:123]
	global_store_dwordx2 v[4:5], v[2:3], off
	ds_read_b128 v[2:5], v181 offset:51200
	s_waitcnt lgkmcnt(0)
	v_lshlrev_b32_e32 v6, 16, v2
	v_and_b32_e32 v2, 0xffff0000, v2
	v_lshlrev_b32_e32 v8, 16, v4
	v_and_b32_e32 v4, 0xffff0000, v4
	v_mul_f32_e32 v2, 0x41800000, v2
	v_lshlrev_b32_e32 v7, 16, v3
	v_med3_f32 v10, v2, s33, v187
	v_mul_f32_e32 v2, 0x41800000, v4
	v_lshlrev_b32_e32 v9, 16, v5
	v_med3_f32 v4, v2, s33, v187
	v_mul_f32_e32 v2, 0x41800000, v7
	v_and_b32_e32 v3, 0xffff0000, v3
	v_med3_f32 v7, v2, s33, v187
	v_mul_f32_e32 v2, 0x41800000, v9
	v_and_b32_e32 v5, 0xffff0000, v5
	v_med3_f32 v9, v2, s33, v187
	v_mul_f32_e32 v2, 0x41800000, v3
	v_mul_f32_e32 v6, 0x41800000, v6
	v_med3_f32 v3, v2, s33, v187
	v_mul_f32_e32 v2, 0x41800000, v5
	v_med3_f32 v6, v6, s33, v187
	v_med3_f32 v5, v2, s33, v187
	v_mov_b32_e32 v2, 0
	v_cvt_pk_fp8_f32 v2, v6, v10
	v_mul_f32_e32 v8, 0x41800000, v8
	v_med3_f32 v8, v8, s33, v187
	v_cvt_pk_fp8_f32 v2, v7, v3 op_sel:[0,0,1]
	v_mov_b32_e32 v3, 0
	v_cvt_pk_fp8_f32 v3, v8, v4
	v_cvt_pk_fp8_f32 v3, v9, v5 op_sel:[0,0,1]
	v_lshl_add_u64 v[4:5], v[0:1], 0, v[124:125]
	global_store_dwordx2 v[4:5], v[2:3], off
	ds_read_b128 v[2:5], v182 offset:51200
	s_waitcnt lgkmcnt(0)
	v_lshlrev_b32_e32 v6, 16, v2
	v_and_b32_e32 v2, 0xffff0000, v2
	v_lshlrev_b32_e32 v8, 16, v4
	v_and_b32_e32 v4, 0xffff0000, v4
	v_mul_f32_e32 v2, 0x41800000, v2
	v_lshlrev_b32_e32 v7, 16, v3
	v_med3_f32 v10, v2, s33, v187
	v_mul_f32_e32 v2, 0x41800000, v4
	v_lshlrev_b32_e32 v9, 16, v5
	v_med3_f32 v4, v2, s33, v187
	v_mul_f32_e32 v2, 0x41800000, v7
	v_and_b32_e32 v3, 0xffff0000, v3
	v_med3_f32 v7, v2, s33, v187
	v_mul_f32_e32 v2, 0x41800000, v9
	v_and_b32_e32 v5, 0xffff0000, v5
	v_med3_f32 v9, v2, s33, v187
	v_mul_f32_e32 v2, 0x41800000, v3
	v_mul_f32_e32 v6, 0x41800000, v6
	v_med3_f32 v3, v2, s33, v187
	v_mul_f32_e32 v2, 0x41800000, v5
	v_med3_f32 v6, v6, s33, v187
	v_med3_f32 v5, v2, s33, v187
	v_mov_b32_e32 v2, 0
	v_cvt_pk_fp8_f32 v2, v6, v10
	v_mul_f32_e32 v8, 0x41800000, v8
	v_med3_f32 v8, v8, s33, v187
	v_cvt_pk_fp8_f32 v2, v7, v3 op_sel:[0,0,1]
	v_mov_b32_e32 v3, 0
	v_cvt_pk_fp8_f32 v3, v8, v4
	v_cvt_pk_fp8_f32 v3, v9, v5 op_sel:[0,0,1]
	v_lshl_add_u64 v[4:5], v[0:1], 0, v[126:127]
	v_lshl_add_u64 v[0:1], v[0:1], 0, v[128:129]
	global_store_dwordx2 v[4:5], v[2:3], off
	ds_read_b128 v[2:5], v183 offset:51200
	s_waitcnt lgkmcnt(0)
	v_lshlrev_b32_e32 v6, 16, v2
	v_and_b32_e32 v2, 0xffff0000, v2
	v_lshlrev_b32_e32 v8, 16, v4
	v_and_b32_e32 v4, 0xffff0000, v4
	v_mul_f32_e32 v2, 0x41800000, v2
	v_lshlrev_b32_e32 v7, 16, v3
	v_med3_f32 v10, v2, s33, v187
	v_mul_f32_e32 v2, 0x41800000, v4
	v_lshlrev_b32_e32 v9, 16, v5
	v_med3_f32 v4, v2, s33, v187
	v_mul_f32_e32 v2, 0x41800000, v7
	v_and_b32_e32 v3, 0xffff0000, v3
	v_med3_f32 v7, v2, s33, v187
	v_mul_f32_e32 v2, 0x41800000, v9
	v_and_b32_e32 v5, 0xffff0000, v5
	v_med3_f32 v9, v2, s33, v187
	v_mul_f32_e32 v2, 0x41800000, v3
	v_mul_f32_e32 v6, 0x41800000, v6
	v_med3_f32 v3, v2, s33, v187
	v_mul_f32_e32 v2, 0x41800000, v5
	v_med3_f32 v6, v6, s33, v187
	v_med3_f32 v5, v2, s33, v187
	v_mov_b32_e32 v2, 0
	v_cvt_pk_fp8_f32 v2, v6, v10
	v_mul_f32_e32 v8, 0x41800000, v8
	v_med3_f32 v8, v8, s33, v187
	v_cvt_pk_fp8_f32 v2, v7, v3 op_sel:[0,0,1]
	v_mov_b32_e32 v3, 0
	v_cvt_pk_fp8_f32 v3, v8, v4
	v_cvt_pk_fp8_f32 v3, v9, v5 op_sel:[0,0,1]
	global_store_dwordx2 v[0:1], v[2:3], off
	s_waitcnt lgkmcnt(0)
	s_barrier
	s_and_saveexec_b64 s[38:39], s[2:3]
	s_cbranch_execz .LBB0_1400
	v_mov_b32_e32 v0, s18
	ds_write_b32 v0, v188
	s_branch .LBB0_1400

.LBB0_2302:
	s_mov_b64 s[8:9], exec
	v_readlane_b32 s10, v255, 4
	v_readlane_b32 s11, v255, 5
	s_and_b64 s[10:11], s[8:9], s[10:11]
	s_mov_b64 exec, s[10:11]
	v_mov_b32_e32 v32, 1.0
	ds_write_b32 v178, v32 offset:49152
	s_or_b64 exec, exec, s[8:9]
	s_waitcnt lgkmcnt(0)
	ds_read_b32 v64, v180 offset:49152
	ds_read_b32 v65, v180 offset:49156
	ds_read_b32 v66, v182 offset:49152
	ds_read_b32 v67, v183 offset:49152
	ds_read_b32 v68, v184 offset:49152
	ds_read_b32 v69, v185 offset:49152
	ds_read_b32 v70, v186 offset:49152
	ds_read_b32 v71, v187 offset:49152
	ds_read_b32 v72, v180 offset:49216
	ds_read_b32 v73, v180 offset:49220
	ds_read_b32 v74, v180 offset:49224
	ds_read_b32 v75, v180 offset:49228
	ds_read_b32 v76, v180 offset:49248
	ds_read_b32 v77, v180 offset:49252
	ds_read_b32 v78, v180 offset:49256
	ds_read_b32 v79, v180 offset:49260
	v_add_u32_e32 v33, v179, v181
	s_lshl_b32 s8, s79, 10
	v_readlane_b32 s9, v254, 48
	s_add_u32 s8, s9, s8
	s_waitcnt lgkmcnt(0)
	v_mul_f32_e32 v0, v0, v64
	v_mul_f32_e32 v16, v16, v64
	v_cvt_pk_bf16_f32 v0, v0, v157
	ds_write_b16 v33, v0 offset:51200
	v_cvt_pk_bf16_f32 v0, v16, v157
	ds_write_b16 v33, v0 offset:51264
	v_readlane_b32 s9, v254, 49
	s_addc_u32 s9, s9, 0
	s_add_u32 s10, s8, s78
	v_mul_f32_e32 v0, v1, v65
	v_mul_f32_e32 v1, v17, v65
	v_cvt_pk_bf16_f32 v0, v0, v157
	ds_write_b16 v190, v0 offset:51200
	v_cvt_pk_bf16_f32 v0, v1, v157
	ds_write_b16 v190, v0 offset:51264
	s_addc_u32 s11, s9, 0
	s_lshl_b64 s[8:9], s[0:1], 10
	s_add_u32 s8, s10, s8
	v_mul_f32_e32 v0, v2, v66
	v_mul_f32_e32 v1, v18, v66
	v_cvt_pk_bf16_f32 v0, v0, v157
	ds_write_b16 v191, v0 offset:51200
	v_cvt_pk_bf16_f32 v0, v1, v157
	ds_write_b16 v191, v0 offset:51264
	s_addc_u32 s9, s11, s9
	v_mul_f32_e32 v0, v3, v67
	v_mul_f32_e32 v1, v19, v67
	v_cvt_pk_bf16_f32 v0, v0, v157
	ds_write_b16 v192, v0 offset:51200
	v_cvt_pk_bf16_f32 v0, v1, v157
	ds_write_b16 v192, v0 offset:51264
	v_mul_f32_e32 v0, v4, v68
	v_mul_f32_e32 v1, v20, v68
	v_cvt_pk_bf16_f32 v0, v0, v157
	ds_write_b16 v193, v0 offset:51200
	v_cvt_pk_bf16_f32 v0, v1, v157
	ds_write_b16 v193, v0 offset:51264
	v_mul_f32_e32 v0, v5, v69
	v_mul_f32_e32 v1, v21, v69
	v_cvt_pk_bf16_f32 v0, v0, v157
	ds_write_b16 v194, v0 offset:51200
	v_cvt_pk_bf16_f32 v0, v1, v157
	ds_write_b16 v194, v0 offset:51264
	v_mul_f32_e32 v0, v6, v70
	v_mul_f32_e32 v1, v22, v70
	v_cvt_pk_bf16_f32 v0, v0, v157
	ds_write_b16 v195, v0 offset:51200
	v_cvt_pk_bf16_f32 v0, v1, v157
	ds_write_b16 v195, v0 offset:51264
	v_mul_f32_e32 v0, v7, v71
	v_mul_f32_e32 v1, v23, v71
	v_cvt_pk_bf16_f32 v0, v0, v157
	ds_write_b16 v196, v0 offset:51200
	v_cvt_pk_bf16_f32 v0, v1, v157
	ds_write_b16 v196, v0 offset:51264
	v_mul_f32_e32 v0, v8, v72
	v_mul_f32_e32 v1, v24, v72
	v_cvt_pk_bf16_f32 v0, v0, v157
	ds_write_b16 v197, v0 offset:51200
	v_cvt_pk_bf16_f32 v0, v1, v157
	ds_write_b16 v197, v0 offset:51264
	v_mul_f32_e32 v0, v9, v73
	v_mul_f32_e32 v1, v25, v73
	v_cvt_pk_bf16_f32 v0, v0, v157
	ds_write_b16 v198, v0 offset:51200
	v_cvt_pk_bf16_f32 v0, v1, v157
	ds_write_b16 v198, v0 offset:51264
	v_lshl_add_u64 v[8:9], s[8:9], 0, v[160:161]
	v_mul_f32_e32 v0, v10, v74
	v_mul_f32_e32 v1, v26, v74
	v_cvt_pk_bf16_f32 v0, v0, v157
	ds_write_b16 v199, v0 offset:51200
	v_cvt_pk_bf16_f32 v0, v1, v157
	ds_write_b16 v199, v0 offset:51264
	v_mul_f32_e32 v0, v11, v75
	v_mul_f32_e32 v1, v27, v75
	v_cvt_pk_bf16_f32 v0, v0, v157
	ds_write_b16 v200, v0 offset:51200
	v_cvt_pk_bf16_f32 v0, v1, v157
	ds_write_b16 v200, v0 offset:51264
	v_mul_f32_e32 v0, v12, v76
	v_mul_f32_e32 v1, v28, v76
	v_cvt_pk_bf16_f32 v0, v0, v157
	ds_write_b16 v201, v0 offset:51200
	v_cvt_pk_bf16_f32 v0, v1, v157
	ds_write_b16 v201, v0 offset:51264
	v_mul_f32_e32 v0, v13, v77
	v_mul_f32_e32 v1, v29, v77
	v_cvt_pk_bf16_f32 v0, v0, v157
	ds_write_b16 v202, v0 offset:51200
	v_cvt_pk_bf16_f32 v0, v1, v157
	ds_write_b16 v202, v0 offset:51264
	v_mul_f32_e32 v0, v14, v78
	v_mul_f32_e32 v1, v30, v78
	v_cvt_pk_bf16_f32 v0, v0, v157
	ds_write_b16 v203, v0 offset:51200
	v_cvt_pk_bf16_f32 v0, v1, v157
	ds_write_b16 v203, v0 offset:51264
	v_mul_f32_e32 v0, v15, v79
	v_cvt_pk_bf16_f32 v0, v0, v157
	ds_write_b16 v204, v0 offset:51200
	v_mul_f32_e32 v0, v31, v79
	v_cvt_pk_bf16_f32 v0, v0, v157
	ds_write_b16 v204, v0 offset:51264
	s_waitcnt lgkmcnt(0)
	ds_read_b128 v[0:3], v205 offset:51200
	ds_read_b128 v[4:7], v206 offset:51200
	s_waitcnt lgkmcnt(0)
	v_lshlrev_b32_e32 v10, 16, v0
	v_lshlrev_b32_e32 v12, 16, v2
	v_mul_f32_e32 v10, 0x41800000, v10
	v_lshlrev_b32_e32 v11, 16, v1
	v_med3_f32 v14, v10, s7, v210
	v_mul_f32_e32 v10, 0x41800000, v12
	v_and_b32_e32 v0, 0xffff0000, v0
	v_and_b32_e32 v2, 0xffff0000, v2
	v_lshlrev_b32_e32 v13, 16, v3
	v_med3_f32 v12, v10, s7, v210
	v_mul_f32_e32 v10, 0x41800000, v11
	v_mul_f32_e32 v0, 0x41800000, v0
	v_mul_f32_e32 v2, 0x41800000, v2
	v_med3_f32 v15, v10, s7, v210
	v_mul_f32_e32 v10, 0x41800000, v13
	v_med3_f32 v0, v0, s7, v210
	v_med3_f32 v2, v2, s7, v210
	v_med3_f32 v13, v10, s7, v210
	v_mov_b32_e32 v10, 0
	v_mov_b32_e32 v11, 0
	v_cvt_pk_fp8_f32 v10, v14, v0
	v_cvt_pk_fp8_f32 v11, v12, v2
	v_and_b32_e32 v1, 0xffff0000, v1
	v_and_b32_e32 v3, 0xffff0000, v3
	v_mul_f32_e32 v1, 0x41800000, v1
	v_mul_f32_e32 v0, 0x41800000, v3
	v_med3_f32 v1, v1, s7, v210
	v_med3_f32 v0, v0, s7, v210
	v_cvt_pk_fp8_f32 v10, v15, v1 op_sel:[0,0,1]
	v_cvt_pk_fp8_f32 v11, v13, v0 op_sel:[0,0,1]
	v_lshlrev_b32_e32 v0, 16, v4
	v_and_b32_e32 v1, 0xffff0000, v4
	v_lshlrev_b32_e32 v4, 16, v6
	v_lshlrev_b32_e32 v2, 16, v5
	v_and_b32_e32 v3, 0xffff0000, v5
	v_and_b32_e32 v5, 0xffff0000, v6
	v_mul_f32_e32 v4, 0x41800000, v4
	v_lshlrev_b32_e32 v6, 16, v7
	v_med3_f32 v14, v4, s7, v210
	v_mul_f32_e32 v4, 0x41800000, v5
	v_mul_f32_e32 v0, 0x41800000, v0
	v_mul_f32_e32 v1, 0x41800000, v1
	v_med3_f32 v15, v4, s7, v210
	v_mul_f32_e32 v4, 0x41800000, v6
	v_med3_f32 v0, v0, s7, v210
	v_med3_f32 v1, v1, s7, v210
	v_med3_f32 v6, v4, s7, v210
	v_mov_b32_e32 v4, 0
	v_mov_b32_e32 v5, 0
	v_cvt_pk_fp8_f32 v4, v0, v1
	v_cvt_pk_fp8_f32 v5, v14, v15
	v_and_b32_e32 v7, 0xffff0000, v7
	v_mul_f32_e32 v2, 0x41800000, v2
	v_mul_f32_e32 v3, 0x41800000, v3
	v_mul_f32_e32 v0, 0x41800000, v7
	v_med3_f32 v2, v2, s7, v210
	v_med3_f32 v3, v3, s7, v210
	v_med3_f32 v0, v0, s7, v210
	v_cvt_pk_fp8_f32 v4, v2, v3 op_sel:[0,0,1]
	v_cvt_pk_fp8_f32 v5, v6, v0 op_sel:[0,0,1]
	ds_read_b128 v[0:3], v207 offset:51200
	v_lshl_add_u64 v[12:13], v[8:9], 0, v[162:163]
	v_lshl_add_u64 v[6:7], v[8:9], 0, v[164:165]
	global_store_dwordx2 v[12:13], v[10:11], off
	global_store_dwordx2 v[6:7], v[4:5], off
	ds_read_b128 v[4:7], v208 offset:51200
	s_waitcnt lgkmcnt(0)
	v_lshlrev_b32_e32 v10, 16, v0
	v_and_b32_e32 v0, 0xffff0000, v0
	v_lshlrev_b32_e32 v12, 16, v2
	v_and_b32_e32 v2, 0xffff0000, v2
	v_mul_f32_e32 v0, 0x41800000, v0
	v_lshlrev_b32_e32 v11, 16, v1
	v_med3_f32 v14, v0, s7, v210
	v_mul_f32_e32 v0, 0x41800000, v2
	v_lshlrev_b32_e32 v13, 16, v3
	v_med3_f32 v2, v0, s7, v210
	v_mul_f32_e32 v0, 0x41800000, v11
	v_and_b32_e32 v1, 0xffff0000, v1
	v_mul_f32_e32 v12, 0x41800000, v12
	v_med3_f32 v11, v0, s7, v210
	v_mul_f32_e32 v0, 0x41800000, v13
	v_med3_f32 v12, v12, s7, v210
	v_med3_f32 v13, v0, s7, v210
	v_mul_f32_e32 v0, 0x41800000, v1
	v_mov_b32_e32 v1, 0
	v_cvt_pk_fp8_f32 v1, v12, v2
	v_and_b32_e32 v3, 0xffff0000, v3
	v_mul_f32_e32 v2, 0x41800000, v3
	v_mul_f32_e32 v10, 0x41800000, v10
	v_med3_f32 v2, v2, s7, v210
	v_med3_f32 v10, v10, s7, v210
	v_med3_f32 v15, v0, s7, v210
	v_mov_b32_e32 v0, 0
	v_cvt_pk_fp8_f32 v1, v13, v2 op_sel:[0,0,1]
	v_lshlrev_b32_e32 v2, 16, v4
	v_cvt_pk_fp8_f32 v0, v10, v14
	v_lshlrev_b32_e32 v10, 16, v6
	v_mul_f32_e32 v2, 0x41800000, v2
	v_and_b32_e32 v3, 0xffff0000, v4
	v_med3_f32 v12, v2, s7, v210
	v_mul_f32_e32 v2, 0x41800000, v10
	v_and_b32_e32 v6, 0xffff0000, v6
	v_med3_f32 v10, v2, s7, v210
	v_mul_f32_e32 v2, 0x41800000, v3
	v_lshlrev_b32_e32 v4, 16, v5
	v_med3_f32 v3, v2, s7, v210
	v_mul_f32_e32 v2, 0x41800000, v6
	v_cvt_pk_fp8_f32 v0, v11, v15 op_sel:[0,0,1]
	v_lshlrev_b32_e32 v11, 16, v7
	v_med3_f32 v6, v2, s7, v210
	v_mul_f32_e32 v2, 0x41800000, v4
	v_and_b32_e32 v5, 0xffff0000, v5
	v_med3_f32 v4, v2, s7, v210
	v_mul_f32_e32 v2, 0x41800000, v11
	v_med3_f32 v11, v2, s7, v210
	v_mul_f32_e32 v2, 0x41800000, v5
	v_med3_f32 v5, v2, s7, v210
	v_mov_b32_e32 v2, 0
	v_cvt_pk_fp8_f32 v2, v12, v3
	v_mov_b32_e32 v3, 0
	v_cvt_pk_fp8_f32 v3, v10, v6
	v_and_b32_e32 v7, 0xffff0000, v7
	v_mul_f32_e32 v6, 0x41800000, v7
	v_med3_f32 v6, v6, s7, v210
	v_cvt_pk_fp8_f32 v2, v4, v5 op_sel:[0,0,1]
	v_cvt_pk_fp8_f32 v3, v11, v6 op_sel:[0,0,1]
	v_lshl_add_u64 v[4:5], v[8:9], 0, v[166:167]
	global_store_dwordx2 v[4:5], v[0:1], off
	v_lshl_add_u64 v[0:1], v[8:9], 0, v[168:169]
	global_store_dwordx2 v[0:1], v[2:3], off
	s_waitcnt vmcnt(0) lgkmcnt(0)
	s_barrier
	s_and_saveexec_b64 s[8:9], s[2:3]
	v_readlane_b32 s74, v254, 58
	s_cbranch_execz .LBB0_2277
	v_readlane_b32 s0, v254, 6
	s_nop 1
	v_mov_b32_e32 v0, s0
	ds_write_b32 v0, v211
	s_branch .LBB0_2277

.LBB0_3054:
	s_or_b64 exec, exec, s[0:1]
	s_waitcnt lgkmcnt(0)
	ds_read_b32 v64, v168 offset:49152
	ds_read_b32 v65, v168 offset:49156
	ds_read_b32 v66, v168 offset:49160
	ds_read_b32 v67, v168 offset:49164
	ds_read_b32 v68, v168 offset:49184
	ds_read_b32 v69, v168 offset:49188
	ds_read_b32 v70, v168 offset:49192
	ds_read_b32 v71, v168 offset:49196
	ds_read_b32 v72, v168 offset:49216
	ds_read_b32 v73, v168 offset:49220
	ds_read_b32 v74, v168 offset:49224
	ds_read_b32 v75, v168 offset:49228
	ds_read_b32 v76, v168 offset:49248
	ds_read_b32 v77, v168 offset:49252
	ds_read_b32 v78, v168 offset:49256
	ds_read_b32 v79, v168 offset:49260
	v_add_u32_e32 v33, v169, v170
	s_lshl_b32 s0, s50, 10
	v_readlane_b32 s1, v254, 48
	s_add_u32 s0, s1, s0
	s_waitcnt lgkmcnt(0)
	v_mul_f32_e32 v0, v0, v64
	v_mul_f32_e32 v16, v16, v64
	v_cvt_pk_bf16_f32 v0, v0, v117
	ds_write_b16 v33, v0 offset:51200
	v_cvt_pk_bf16_f32 v0, v16, v117
	ds_write_b16 v33, v0 offset:51264
	v_readlane_b32 s1, v254, 49
	s_addc_u32 s1, s1, 0
	s_add_u32 s6, s0, s51
	v_mul_f32_e32 v0, v1, v65
	v_mul_f32_e32 v1, v17, v65
	v_cvt_pk_bf16_f32 v0, v0, v117
	ds_write_b16 v172, v0 offset:51200
	v_cvt_pk_bf16_f32 v0, v1, v117
	ds_write_b16 v172, v0 offset:51264
	s_addc_u32 s7, s1, 0
	s_lshl_b64 s[0:1], s[8:9], 10
	s_add_u32 s0, s6, s0
	v_mul_f32_e32 v0, v2, v66
	v_mul_f32_e32 v1, v18, v66
	v_cvt_pk_bf16_f32 v0, v0, v117
	ds_write_b16 v173, v0 offset:51200
	v_cvt_pk_bf16_f32 v0, v1, v117
	ds_write_b16 v173, v0 offset:51264
	s_addc_u32 s1, s7, s1
	v_mul_f32_e32 v0, v3, v67
	v_mul_f32_e32 v1, v19, v67
	v_cvt_pk_bf16_f32 v0, v0, v117
	ds_write_b16 v174, v0 offset:51200
	v_cvt_pk_bf16_f32 v0, v1, v117
	ds_write_b16 v174, v0 offset:51264
	v_mul_f32_e32 v0, v4, v68
	v_mul_f32_e32 v1, v20, v68
	v_cvt_pk_bf16_f32 v0, v0, v117
	ds_write_b16 v175, v0 offset:51200
	v_cvt_pk_bf16_f32 v0, v1, v117
	ds_write_b16 v175, v0 offset:51264
	v_mul_f32_e32 v0, v5, v69
	v_mul_f32_e32 v1, v21, v69
	v_cvt_pk_bf16_f32 v0, v0, v117
	ds_write_b16 v176, v0 offset:51200
	v_cvt_pk_bf16_f32 v0, v1, v117
	ds_write_b16 v176, v0 offset:51264
	v_mul_f32_e32 v0, v6, v70
	v_mul_f32_e32 v1, v22, v70
	v_cvt_pk_bf16_f32 v0, v0, v117
	ds_write_b16 v177, v0 offset:51200
	v_cvt_pk_bf16_f32 v0, v1, v117
	ds_write_b16 v177, v0 offset:51264
	v_mul_f32_e32 v0, v7, v71
	v_mul_f32_e32 v1, v23, v71
	v_cvt_pk_bf16_f32 v0, v0, v117
	ds_write_b16 v178, v0 offset:51200
	v_cvt_pk_bf16_f32 v0, v1, v117
	ds_write_b16 v178, v0 offset:51264
	v_mul_f32_e32 v0, v8, v72
	v_mul_f32_e32 v1, v24, v72
	v_cvt_pk_bf16_f32 v0, v0, v117
	ds_write_b16 v179, v0 offset:51200
	v_cvt_pk_bf16_f32 v0, v1, v117
	ds_write_b16 v179, v0 offset:51264
	v_mul_f32_e32 v0, v9, v73
	v_mul_f32_e32 v1, v25, v73
	v_cvt_pk_bf16_f32 v0, v0, v117
	ds_write_b16 v180, v0 offset:51200
	v_cvt_pk_bf16_f32 v0, v1, v117
	ds_write_b16 v180, v0 offset:51264
	v_lshl_add_u64 v[8:9], s[0:1], 0, v[122:123]
	v_mul_f32_e32 v0, v10, v74
	v_mul_f32_e32 v1, v26, v74
	v_cvt_pk_bf16_f32 v0, v0, v117
	ds_write_b16 v181, v0 offset:51200
	v_cvt_pk_bf16_f32 v0, v1, v117
	ds_write_b16 v181, v0 offset:51264
	v_mul_f32_e32 v0, v11, v75
	v_mul_f32_e32 v1, v27, v75
	v_cvt_pk_bf16_f32 v0, v0, v117
	ds_write_b16 v182, v0 offset:51200
	v_cvt_pk_bf16_f32 v0, v1, v117
	ds_write_b16 v182, v0 offset:51264
	v_mul_f32_e32 v0, v12, v76
	v_mul_f32_e32 v1, v28, v76
	v_cvt_pk_bf16_f32 v0, v0, v117
	ds_write_b16 v183, v0 offset:51200
	v_cvt_pk_bf16_f32 v0, v1, v117
	ds_write_b16 v183, v0 offset:51264
	v_mul_f32_e32 v0, v13, v77
	v_mul_f32_e32 v1, v29, v77
	v_cvt_pk_bf16_f32 v0, v0, v117
	ds_write_b16 v184, v0 offset:51200
	v_cvt_pk_bf16_f32 v0, v1, v117
	ds_write_b16 v184, v0 offset:51264
	v_mul_f32_e32 v0, v14, v78
	v_mul_f32_e32 v1, v30, v78
	v_cvt_pk_bf16_f32 v0, v0, v117
	ds_write_b16 v185, v0 offset:51200
	v_cvt_pk_bf16_f32 v0, v1, v117
	ds_write_b16 v185, v0 offset:51264
	v_mul_f32_e32 v0, v15, v79
	v_cvt_pk_bf16_f32 v0, v0, v117
	ds_write_b16 v186, v0 offset:51200
	v_mul_f32_e32 v0, v31, v79
	v_cvt_pk_bf16_f32 v0, v0, v117
	ds_write_b16 v186, v0 offset:51264
	s_waitcnt lgkmcnt(0)
	ds_read_b128 v[0:3], v187 offset:51200
	ds_read_b128 v[4:7], v188 offset:51200
	s_waitcnt lgkmcnt(0)
	v_lshlrev_b32_e32 v10, 16, v0
	v_lshlrev_b32_e32 v12, 16, v2
	v_mul_f32_e32 v10, 0x41800000, v10
	v_lshlrev_b32_e32 v11, 16, v1
	v_med3_f32 v14, v10, s49, v193
	v_mul_f32_e32 v10, 0x41800000, v12
	v_and_b32_e32 v0, 0xffff0000, v0
	v_and_b32_e32 v2, 0xffff0000, v2
	v_lshlrev_b32_e32 v13, 16, v3
	v_med3_f32 v12, v10, s49, v193
	v_mul_f32_e32 v10, 0x41800000, v11
	v_mul_f32_e32 v0, 0x41800000, v0
	v_mul_f32_e32 v2, 0x41800000, v2
	v_med3_f32 v15, v10, s49, v193
	v_mul_f32_e32 v10, 0x41800000, v13
	v_med3_f32 v0, v0, s49, v193
	v_med3_f32 v2, v2, s49, v193
	v_med3_f32 v13, v10, s49, v193
	v_mov_b32_e32 v10, 0
	v_mov_b32_e32 v11, 0
	v_cvt_pk_fp8_f32 v10, v14, v0
	v_cvt_pk_fp8_f32 v11, v12, v2
	v_and_b32_e32 v1, 0xffff0000, v1
	v_and_b32_e32 v3, 0xffff0000, v3
	v_mul_f32_e32 v1, 0x41800000, v1
	v_mul_f32_e32 v0, 0x41800000, v3
	v_med3_f32 v1, v1, s49, v193
	v_med3_f32 v0, v0, s49, v193
	v_cvt_pk_fp8_f32 v10, v15, v1 op_sel:[0,0,1]
	v_cvt_pk_fp8_f32 v11, v13, v0 op_sel:[0,0,1]
	v_lshlrev_b32_e32 v0, 16, v4
	v_and_b32_e32 v1, 0xffff0000, v4
	v_lshlrev_b32_e32 v4, 16, v6
	v_lshlrev_b32_e32 v2, 16, v5
	v_and_b32_e32 v3, 0xffff0000, v5
	v_and_b32_e32 v5, 0xffff0000, v6
	v_mul_f32_e32 v4, 0x41800000, v4
	v_lshlrev_b32_e32 v6, 16, v7
	v_med3_f32 v14, v4, s49, v193
	v_mul_f32_e32 v4, 0x41800000, v5
	v_mul_f32_e32 v0, 0x41800000, v0
	v_mul_f32_e32 v1, 0x41800000, v1
	v_med3_f32 v15, v4, s49, v193
	v_mul_f32_e32 v4, 0x41800000, v6
	v_med3_f32 v0, v0, s49, v193
	v_med3_f32 v1, v1, s49, v193
	v_med3_f32 v6, v4, s49, v193
	v_mov_b32_e32 v4, 0
	v_mov_b32_e32 v5, 0
	v_cvt_pk_fp8_f32 v4, v0, v1
	v_cvt_pk_fp8_f32 v5, v14, v15
	v_and_b32_e32 v7, 0xffff0000, v7
	v_mul_f32_e32 v2, 0x41800000, v2
	v_mul_f32_e32 v3, 0x41800000, v3
	v_mul_f32_e32 v0, 0x41800000, v7
	v_med3_f32 v2, v2, s49, v193
	v_med3_f32 v3, v3, s49, v193
	v_med3_f32 v0, v0, s49, v193
	v_cvt_pk_fp8_f32 v4, v2, v3 op_sel:[0,0,1]
	v_cvt_pk_fp8_f32 v5, v6, v0 op_sel:[0,0,1]
	ds_read_b128 v[0:3], v189 offset:51200
	v_lshl_add_u64 v[12:13], v[8:9], 0, v[124:125]
	v_lshl_add_u64 v[6:7], v[8:9], 0, v[126:127]
	global_store_dwordx2 v[12:13], v[10:11], off
	global_store_dwordx2 v[6:7], v[4:5], off
	ds_read_b128 v[4:7], v190 offset:51200
	s_waitcnt lgkmcnt(0)
	v_lshlrev_b32_e32 v10, 16, v0
	v_and_b32_e32 v0, 0xffff0000, v0
	v_lshlrev_b32_e32 v12, 16, v2
	v_and_b32_e32 v2, 0xffff0000, v2
	v_mul_f32_e32 v0, 0x41800000, v0
	v_lshlrev_b32_e32 v11, 16, v1
	v_med3_f32 v14, v0, s49, v193
	v_mul_f32_e32 v0, 0x41800000, v2
	v_lshlrev_b32_e32 v13, 16, v3
	v_med3_f32 v2, v0, s49, v193
	v_mul_f32_e32 v0, 0x41800000, v11
	v_and_b32_e32 v1, 0xffff0000, v1
	v_mul_f32_e32 v12, 0x41800000, v12
	v_med3_f32 v11, v0, s49, v193
	v_mul_f32_e32 v0, 0x41800000, v13
	v_med3_f32 v12, v12, s49, v193
	v_med3_f32 v13, v0, s49, v193
	v_mul_f32_e32 v0, 0x41800000, v1
	v_mov_b32_e32 v1, 0
	v_cvt_pk_fp8_f32 v1, v12, v2
	v_and_b32_e32 v3, 0xffff0000, v3
	v_mul_f32_e32 v2, 0x41800000, v3
	v_mul_f32_e32 v10, 0x41800000, v10
	v_med3_f32 v2, v2, s49, v193
	v_med3_f32 v10, v10, s49, v193
	v_med3_f32 v15, v0, s49, v193
	v_mov_b32_e32 v0, 0
	v_cvt_pk_fp8_f32 v1, v13, v2 op_sel:[0,0,1]
	v_lshlrev_b32_e32 v2, 16, v4
	v_cvt_pk_fp8_f32 v0, v10, v14
	v_lshlrev_b32_e32 v10, 16, v6
	v_mul_f32_e32 v2, 0x41800000, v2
	v_and_b32_e32 v3, 0xffff0000, v4
	v_med3_f32 v12, v2, s49, v193
	v_mul_f32_e32 v2, 0x41800000, v10
	v_and_b32_e32 v6, 0xffff0000, v6
	v_med3_f32 v10, v2, s49, v193
	v_mul_f32_e32 v2, 0x41800000, v3
	v_lshlrev_b32_e32 v4, 16, v5
	v_med3_f32 v3, v2, s49, v193
	v_mul_f32_e32 v2, 0x41800000, v6
	v_cvt_pk_fp8_f32 v0, v11, v15 op_sel:[0,0,1]
	v_lshlrev_b32_e32 v11, 16, v7
	v_med3_f32 v6, v2, s49, v193
	v_mul_f32_e32 v2, 0x41800000, v4
	v_and_b32_e32 v5, 0xffff0000, v5
	v_med3_f32 v4, v2, s49, v193
	v_mul_f32_e32 v2, 0x41800000, v11
	v_med3_f32 v11, v2, s49, v193
	v_mul_f32_e32 v2, 0x41800000, v5
	v_med3_f32 v5, v2, s49, v193
	v_mov_b32_e32 v2, 0
	v_cvt_pk_fp8_f32 v2, v12, v3
	v_mov_b32_e32 v3, 0
	v_cvt_pk_fp8_f32 v3, v10, v6
	v_and_b32_e32 v7, 0xffff0000, v7
	v_mul_f32_e32 v6, 0x41800000, v7
	v_med3_f32 v6, v6, s49, v193
	v_cvt_pk_fp8_f32 v2, v4, v5 op_sel:[0,0,1]
	v_cvt_pk_fp8_f32 v3, v11, v6 op_sel:[0,0,1]
	v_lshl_add_u64 v[4:5], v[8:9], 0, v[128:129]
	global_store_dwordx2 v[4:5], v[0:1], off
	v_lshl_add_u64 v[0:1], v[8:9], 0, v[130:131]
	global_store_dwordx2 v[0:1], v[2:3], off
	s_waitcnt lgkmcnt(0)
	s_barrier
	s_and_saveexec_b64 s[0:1], s[2:3]
	s_cbranch_execz .LBB0_3004
	v_mov_b32_e32 v0, s33
	ds_write_b32 v0, v194
	s_branch .LBB0_3004
